# v19: P8 weight (B) tile stage loads issued at the start of the SP2 load segment (activation tiles stay in the MFMA block) (m1)
# baseline (speedup 1.0000x reference)
.LBB0_901:
	ds_read_b64_tr_b16 v[26:27], v207 offset:0
	ds_read_b64_tr_b16 v[28:29], v207 offset:1024
	ds_read_b64_tr_b16 v[30:31], v207 offset:8192
	ds_read_b64_tr_b16 v[32:33], v207 offset:9216
	ds_read_b64_tr_b16 v[18:19], v217 offset:0
	ds_read_b64_tr_b16 v[20:21], v217 offset:1024
	ds_read_b64_tr_b16 v[22:23], v217 offset:8192
	ds_read_b64_tr_b16 v[24:25], v217 offset:9216
	ds_read_b64_tr_b16 v[10:11], v214 offset:0
	ds_read_b64_tr_b16 v[12:13], v214 offset:1024
	ds_read_b64_tr_b16 v[14:15], v214 offset:8192
	ds_read_b64_tr_b16 v[16:17], v214 offset:9216
	ds_read_b64_tr_b16 v[2:3], v218 offset:0
	ds_read_b64_tr_b16 v[4:5], v218 offset:1024
	ds_read_b64_tr_b16 v[6:7], v218 offset:8192
	ds_read_b64_tr_b16 v[8:9], v218 offset:9216
	s_add_u32 s2, s50, 0xfffc0080
	s_addc_u32 s3, s51, -1
	s_cmp_eq_u32 s72, 12
	s_cselect_b32 s55, s29, s3
	s_cselect_b32 s54, s31, s2
	s_cselect_b32 s53, s35, s71
	s_cselect_b32 s52, s43, s70
	ds_read_b128 v[34:37], v223
	ds_read_b128 v[38:41], v223 offset:1024
	ds_read_b128 v[42:45], v223 offset:2048
	ds_read_b128 v[46:49], v223 offset:3072
	ds_read_b128 v[50:53], v223 offset:4096
	ds_read_b128 v[54:57], v223 offset:5120
	ds_read_b128 v[58:61], v223 offset:6144
	ds_read_b128 v[62:65], v223 offset:7168
	s_waitcnt vmcnt(6)
	s_waitcnt lgkmcnt(0)
	s_barrier
	s_setprio 1
	s_waitcnt lgkmcnt(0)
	v_mfma_scale_f32_16x16x128_f8f6f4 v[194:197], v[26:33], v[34:41], v[194:197], v1, v1 op_sel_hi:[0,0,0]
	v_mfma_scale_f32_16x16x128_f8f6f4 v[190:193], v[18:25], v[34:41], v[190:193], v1, v1 op_sel_hi:[0,0,0]
	v_mfma_scale_f32_16x16x128_f8f6f4 v[186:189], v[26:33], v[42:49], v[186:189], v1, v1 op_sel_hi:[0,0,0]
	v_mfma_scale_f32_16x16x128_f8f6f4 v[182:185], v[18:25], v[42:49], v[182:185], v1, v1 op_sel_hi:[0,0,0]
	v_lshl_add_u64 v[68:69], s[50:51], 0, v[208:209]
	s_add_i32 m0, s17, 0xc000
	s_nop 0
	global_load_lds_dwordx4 v[68:69], off
	v_mfma_scale_f32_16x16x128_f8f6f4 v[162:165], v[26:33], v[50:57], v[162:165], v1, v1 op_sel_hi:[0,0,0]
	v_mfma_scale_f32_16x16x128_f8f6f4 v[158:161], v[18:25], v[50:57], v[158:161], v1, v1 op_sel_hi:[0,0,0]
	v_mfma_scale_f32_16x16x128_f8f6f4 v[146:149], v[26:33], v[58:65], v[146:149], v1, v1 op_sel_hi:[0,0,0]
	v_mfma_scale_f32_16x16x128_f8f6f4 v[142:145], v[18:25], v[58:65], v[142:145], v1, v1 op_sel_hi:[0,0,0]
	s_setprio 0
	s_setprio 1
	v_mfma_scale_f32_16x16x128_f8f6f4 v[178:181], v[10:17], v[34:41], v[178:181], v1, v1 op_sel_hi:[0,0,0]
	v_mfma_scale_f32_16x16x128_f8f6f4 v[174:177], v[2:9], v[34:41], v[174:177], v1, v1 op_sel_hi:[0,0,0]
	v_lshl_add_u64 v[68:69], s[50:51], 0, v[210:211]
	s_add_i32 m0, s17, 0xe000
	s_nop 0
	global_load_lds_dwordx4 v[68:69], off
	v_mfma_scale_f32_16x16x128_f8f6f4 v[170:173], v[10:17], v[42:49], v[170:173], v1, v1 op_sel_hi:[0,0,0]
	v_mfma_scale_f32_16x16x128_f8f6f4 v[166:169], v[2:9], v[42:49], v[166:169], v1, v1 op_sel_hi:[0,0,0]
	v_mfma_scale_f32_16x16x128_f8f6f4 v[154:157], v[10:17], v[50:57], v[154:157], v1, v1 op_sel_hi:[0,0,0]
	v_mfma_scale_f32_16x16x128_f8f6f4 v[150:153], v[2:9], v[50:57], v[150:153], v1, v1 op_sel_hi:[0,0,0]
	v_mfma_scale_f32_16x16x128_f8f6f4 v[138:141], v[10:17], v[58:65], v[138:141], v1, v1 op_sel_hi:[0,0,0]
	v_mfma_scale_f32_16x16x128_f8f6f4 v[134:137], v[2:9], v[58:65], v[134:137], v1, v1 op_sel_hi:[0,0,0]
	s_setprio 0
	s_barrier
	s_mov_b32 m0, s19
	v_lshl_add_u64 v[68:69], s[52:53], 0, v[200:201]
	global_load_lds_dwordx4 v[68:69], off
	v_lshl_add_u64 v[212:213], s[52:53], 0, v[204:205]
	s_mov_b32 m0, s33
	v_lshl_add_u64 v[68:69], v[68:69], 0, s[4:5]
	global_load_lds_dwordx4 v[212:213], off
	s_mov_b32 m0, s45
	s_nop 0
	global_load_lds_dwordx4 v[68:69], off
	v_lshl_add_u64 v[68:69], v[212:213], 0, s[4:5]
	s_mov_b32 m0, s47
	v_lshl_add_u64 v[212:213], s[54:55], 0, v[202:203]
	global_load_lds_dwordx4 v[68:69], off
	s_andn2_b64 vcc, exec, s[48:49]
	s_cbranch_vccnz .Lhalfskip_p8a
	ds_read_b128 v[58:61], v223 offset:16384
	ds_read_b128 v[62:65], v223 offset:17408
	ds_read_b128 v[50:53], v223 offset:18432
	ds_read_b128 v[54:57], v223 offset:19456
	ds_read_b128 v[42:45], v223 offset:20480
	ds_read_b128 v[46:49], v223 offset:21504
	ds_read_b128 v[34:37], v223 offset:22528
	ds_read_b128 v[38:41], v223 offset:23552
.Lhalfskip_p8a:
	v_cmp_ne_u32_e64 s[2:3], 1, v225
	s_waitcnt vmcnt(6)
	s_waitcnt lgkmcnt(0)
	s_barrier
	s_cbranch_vccnz .Lp8_skip_b
	s_setprio 1
	s_waitcnt lgkmcnt(0)
	v_mfma_scale_f32_16x16x128_f8f6f4 v[130:133], v[26:33], v[58:65], v[130:133], v1, v1 op_sel_hi:[0,0,0]
	v_mfma_scale_f32_16x16x128_f8f6f4 v[126:129], v[18:25], v[58:65], v[126:129], v1, v1 op_sel_hi:[0,0,0]
	v_mfma_scale_f32_16x16x128_f8f6f4 v[114:117], v[26:33], v[50:57], v[114:117], v1, v1 op_sel_hi:[0,0,0]
	v_mfma_scale_f32_16x16x128_f8f6f4 v[110:113], v[18:25], v[50:57], v[110:113], v1, v1 op_sel_hi:[0,0,0]
	v_mfma_scale_f32_16x16x128_f8f6f4 v[98:101], v[26:33], v[42:49], v[98:101], v1, v1 op_sel_hi:[0,0,0]
	v_mfma_scale_f32_16x16x128_f8f6f4 v[94:97], v[18:25], v[42:49], v[94:97], v1, v1 op_sel_hi:[0,0,0]
	v_mfma_scale_f32_16x16x128_f8f6f4 v[82:85], v[26:33], v[34:41], v[82:85], v1, v1 op_sel_hi:[0,0,0]
	v_mfma_scale_f32_16x16x128_f8f6f4 v[78:81], v[18:25], v[34:41], v[78:81], v1, v1 op_sel_hi:[0,0,0]
	s_setprio 0
	s_setprio 1
	v_mfma_scale_f32_16x16x128_f8f6f4 v[122:125], v[10:17], v[58:65], v[122:125], v1, v1 op_sel_hi:[0,0,0]
	v_mfma_scale_f32_16x16x128_f8f6f4 v[118:121], v[2:9], v[58:65], v[118:121], v1, v1 op_sel_hi:[0,0,0]
	v_mfma_scale_f32_16x16x128_f8f6f4 v[106:109], v[10:17], v[50:57], v[106:109], v1, v1 op_sel_hi:[0,0,0]
	v_lshl_add_u64 v[68:69], s[54:55], 0, v[198:199]
	s_mov_b32 m0, s17
	s_nop 0
	global_load_lds_dwordx4 v[68:69], off
	v_mfma_scale_f32_16x16x128_f8f6f4 v[102:105], v[2:9], v[50:57], v[102:105], v1, v1 op_sel_hi:[0,0,0]
	v_mfma_scale_f32_16x16x128_f8f6f4 v[90:93], v[10:17], v[42:49], v[90:93], v1, v1 op_sel_hi:[0,0,0]
	s_mov_b32 m0, s58
	s_nop 0
	global_load_lds_dwordx4 v[212:213], off
	v_mfma_scale_f32_16x16x128_f8f6f4 v[86:89], v[2:9], v[42:49], v[86:89], v1, v1 op_sel_hi:[0,0,0]
	v_mfma_scale_f32_16x16x128_f8f6f4 v[74:77], v[10:17], v[34:41], v[74:77], v1, v1 op_sel_hi:[0,0,0]
	v_mfma_scale_f32_16x16x128_f8f6f4 v[70:73], v[2:9], v[34:41], v[70:73], v1, v1 op_sel_hi:[0,0,0]
	s_setprio 0
.LBB0_903:
	s_add_u32 s56, s52, 0x40000
	s_addc_u32 s57, s53, 0
	s_barrier
	ds_read_b64_tr_b16 v[26:27], v215 offset:0
	ds_read_b64_tr_b16 v[28:29], v215 offset:1024
	ds_read_b64_tr_b16 v[30:31], v215 offset:8192
	ds_read_b64_tr_b16 v[32:33], v215 offset:9216
	ds_read_b64_tr_b16 v[18:19], v219 offset:0
	ds_read_b64_tr_b16 v[20:21], v219 offset:1024
	ds_read_b64_tr_b16 v[22:23], v219 offset:8192
	ds_read_b64_tr_b16 v[24:25], v219 offset:9216
	ds_read_b64_tr_b16 v[10:11], v216 offset:0
	ds_read_b64_tr_b16 v[12:13], v216 offset:1024
	ds_read_b64_tr_b16 v[14:15], v216 offset:8192
	ds_read_b64_tr_b16 v[16:17], v216 offset:9216
	ds_read_b64_tr_b16 v[2:3], v220 offset:0
	ds_read_b64_tr_b16 v[4:5], v220 offset:1024
	ds_read_b64_tr_b16 v[6:7], v220 offset:8192
	ds_read_b64_tr_b16 v[8:9], v220 offset:9216
	s_add_u32 s54, s54, 0x40000
	s_addc_u32 s55, s55, 0
	ds_read_b128 v[34:37], v223 offset:32768
	ds_read_b128 v[38:41], v223 offset:33792
	ds_read_b128 v[42:45], v223 offset:34816
	ds_read_b128 v[46:49], v223 offset:35840
	ds_read_b128 v[50:53], v223 offset:36864
	ds_read_b128 v[54:57], v223 offset:37888
	ds_read_b128 v[58:61], v223 offset:38912
	ds_read_b128 v[62:65], v223 offset:39936
	s_waitcnt vmcnt(6)
	s_waitcnt lgkmcnt(0)
	s_barrier
	s_setprio 1
	s_waitcnt lgkmcnt(0)
	v_mfma_scale_f32_16x16x128_f8f6f4 v[194:197], v[26:33], v[34:41], v[194:197], v1, v1 op_sel_hi:[0,0,0]
	v_mfma_scale_f32_16x16x128_f8f6f4 v[190:193], v[18:25], v[34:41], v[190:193], v1, v1 op_sel_hi:[0,0,0]
	v_mfma_scale_f32_16x16x128_f8f6f4 v[186:189], v[26:33], v[42:49], v[186:189], v1, v1 op_sel_hi:[0,0,0]
	v_mfma_scale_f32_16x16x128_f8f6f4 v[182:185], v[18:25], v[42:49], v[182:185], v1, v1 op_sel_hi:[0,0,0]
	s_mov_b32 m0, s59
	v_lshl_add_u64 v[226:227], s[54:55], 0, v[198:199]
	global_load_lds_dwordx4 v[226:227], off
	v_mfma_scale_f32_16x16x128_f8f6f4 v[162:165], v[26:33], v[50:57], v[162:165], v1, v1 op_sel_hi:[0,0,0]
	v_mfma_scale_f32_16x16x128_f8f6f4 v[158:161], v[18:25], v[50:57], v[158:161], v1, v1 op_sel_hi:[0,0,0]
	v_mfma_scale_f32_16x16x128_f8f6f4 v[146:149], v[26:33], v[58:65], v[146:149], v1, v1 op_sel_hi:[0,0,0]
	v_mfma_scale_f32_16x16x128_f8f6f4 v[142:145], v[18:25], v[58:65], v[142:145], v1, v1 op_sel_hi:[0,0,0]
	s_setprio 0
	s_setprio 1
	v_mfma_scale_f32_16x16x128_f8f6f4 v[178:181], v[10:17], v[34:41], v[178:181], v1, v1 op_sel_hi:[0,0,0]
	v_mfma_scale_f32_16x16x128_f8f6f4 v[174:177], v[2:9], v[34:41], v[174:177], v1, v1 op_sel_hi:[0,0,0]
	v_lshl_add_u64 v[226:227], s[54:55], 0, v[202:203]
	s_mov_b32 m0, s60
	s_nop 0
	global_load_lds_dwordx4 v[226:227], off
	v_mfma_scale_f32_16x16x128_f8f6f4 v[170:173], v[10:17], v[42:49], v[170:173], v1, v1 op_sel_hi:[0,0,0]
	v_mfma_scale_f32_16x16x128_f8f6f4 v[166:169], v[2:9], v[42:49], v[166:169], v1, v1 op_sel_hi:[0,0,0]
	v_mfma_scale_f32_16x16x128_f8f6f4 v[154:157], v[10:17], v[50:57], v[154:157], v1, v1 op_sel_hi:[0,0,0]
	v_mfma_scale_f32_16x16x128_f8f6f4 v[150:153], v[2:9], v[50:57], v[150:153], v1, v1 op_sel_hi:[0,0,0]
	v_mfma_scale_f32_16x16x128_f8f6f4 v[138:141], v[10:17], v[58:65], v[138:141], v1, v1 op_sel_hi:[0,0,0]
	v_mfma_scale_f32_16x16x128_f8f6f4 v[134:137], v[2:9], v[58:65], v[134:137], v1, v1 op_sel_hi:[0,0,0]
	s_setprio 0
	s_barrier
	v_lshl_add_u64 v[226:227], s[56:57], 0, v[200:201]
	s_add_i32 m0, s17, 0x18000
	s_nop 0
	global_load_lds_dwordx4 v[226:227], off
	s_add_i32 m0, s17, 0x1a000
	v_lshl_add_u64 v[226:227], s[56:57], 0, v[204:205]
	global_load_lds_dwordx4 v[226:227], off
	s_add_u32 s52, s52, 0x40100
	s_addc_u32 s53, s53, 0
	v_lshl_add_u64 v[226:227], s[52:53], 0, v[200:201]
	s_add_i32 m0, s17, 0x1c000
	v_lshl_add_u64 v[68:69], v[68:69], 0, s[12:13]
	global_load_lds_dwordx4 v[226:227], off
	v_lshl_add_u64 v[226:227], s[52:53], 0, v[204:205]
	s_add_i32 m0, s17, 0x1e000
	s_nop 0
	global_load_lds_dwordx4 v[226:227], off
	s_and_b64 vcc, exec, s[2:3]
	s_cbranch_vccnz .Lhalfskip_p8b
	ds_read_b128 v[58:61], v223 offset:49152
	ds_read_b128 v[62:65], v223 offset:50176
	ds_read_b128 v[50:53], v223 offset:51200
	ds_read_b128 v[54:57], v223 offset:52224
	ds_read_b128 v[42:45], v223 offset:53248
	ds_read_b128 v[46:49], v223 offset:54272
	ds_read_b128 v[34:37], v223 offset:55296
	ds_read_b128 v[38:41], v223 offset:56320
.Lhalfskip_p8b:
	s_waitcnt vmcnt(6)
	s_waitcnt lgkmcnt(0)
	s_barrier
	s_cbranch_vccnz .Lp8_skip_d
	s_setprio 1
	s_waitcnt lgkmcnt(0)
	v_mfma_scale_f32_16x16x128_f8f6f4 v[130:133], v[26:33], v[58:65], v[130:133], v1, v1 op_sel_hi:[0,0,0]
	v_mfma_scale_f32_16x16x128_f8f6f4 v[126:129], v[18:25], v[58:65], v[126:129], v1, v1 op_sel_hi:[0,0,0]
	v_mfma_scale_f32_16x16x128_f8f6f4 v[114:117], v[26:33], v[50:57], v[114:117], v1, v1 op_sel_hi:[0,0,0]
	v_mfma_scale_f32_16x16x128_f8f6f4 v[110:113], v[18:25], v[50:57], v[110:113], v1, v1 op_sel_hi:[0,0,0]
	v_mfma_scale_f32_16x16x128_f8f6f4 v[98:101], v[26:33], v[42:49], v[98:101], v1, v1 op_sel_hi:[0,0,0]
	v_mfma_scale_f32_16x16x128_f8f6f4 v[94:97], v[18:25], v[42:49], v[94:97], v1, v1 op_sel_hi:[0,0,0]
	v_mfma_scale_f32_16x16x128_f8f6f4 v[82:85], v[26:33], v[34:41], v[82:85], v1, v1 op_sel_hi:[0,0,0]
	v_mfma_scale_f32_16x16x128_f8f6f4 v[78:81], v[18:25], v[34:41], v[78:81], v1, v1 op_sel_hi:[0,0,0]
	s_setprio 0
	s_setprio 1
	v_mfma_scale_f32_16x16x128_f8f6f4 v[122:125], v[10:17], v[58:65], v[122:125], v1, v1 op_sel_hi:[0,0,0]
	v_mfma_scale_f32_16x16x128_f8f6f4 v[118:121], v[2:9], v[58:65], v[118:121], v1, v1 op_sel_hi:[0,0,0]
	v_mfma_scale_f32_16x16x128_f8f6f4 v[106:109], v[10:17], v[50:57], v[106:109], v1, v1 op_sel_hi:[0,0,0]
	s_mov_b32 m0, s62
	s_nop 0
	global_load_lds_dwordx4 v[68:69], off
	v_mfma_scale_f32_16x16x128_f8f6f4 v[102:105], v[2:9], v[50:57], v[102:105], v1, v1 op_sel_hi:[0,0,0]
	v_mfma_scale_f32_16x16x128_f8f6f4 v[90:93], v[10:17], v[42:49], v[90:93], v1, v1 op_sel_hi:[0,0,0]
	v_lshl_add_u64 v[68:69], v[212:213], 0, s[12:13]
	s_mov_b32 m0, s63
	s_nop 0
	global_load_lds_dwordx4 v[68:69], off
	v_mfma_scale_f32_16x16x128_f8f6f4 v[86:89], v[2:9], v[42:49], v[86:89], v1, v1 op_sel_hi:[0,0,0]
	v_mfma_scale_f32_16x16x128_f8f6f4 v[74:77], v[10:17], v[34:41], v[74:77], v1, v1 op_sel_hi:[0,0,0]
	v_mfma_scale_f32_16x16x128_f8f6f4 v[70:73], v[2:9], v[34:41], v[70:73], v1, v1 op_sel_hi:[0,0,0]
	s_setprio 0
	s_branch .LBB0_900
.Lp8_skip_b:
	v_lshl_add_u64 v[68:69], s[54:55], 0, v[198:199]
	s_mov_b32 m0, s17
	s_nop 0
	global_load_lds_dwordx4 v[68:69], off
	s_mov_b32 m0, s58
	s_nop 0
	global_load_lds_dwordx4 v[212:213], off
	s_branch .LBB0_903
.Lp8_skip_d:
	s_mov_b32 m0, s62
	s_nop 0
	global_load_lds_dwordx4 v[68:69], off
	v_lshl_add_u64 v[68:69], v[212:213], 0, s[12:13]
	s_mov_b32 m0, s63
	s_nop 0
	global_load_lds_dwordx4 v[68:69], off
	s_branch .LBB0_900
